# baseline (speedup 1.0000x reference)
.Lattn_prio_done:
	.p2align 6
